# v91 with the required wait state restored behind eight M0 writes (hazard table row 16) that the removed address adds used to supply
# baseline (speedup 1.0000x reference)
.Lp1_blk3:
	ds_read_b128 v[184:187], v175 offset:32768
	ds_read_b128 v[188:191], v176 offset:32768
	ds_read_b128 v[192:195], v175 offset:34816
	ds_read_b128 v[196:199], v176 offset:34816
	ds_read_b128 v[200:203], v175 offset:49152
	ds_read_b128 v[204:207], v176 offset:49152
	ds_read_b128 v[208:211], v175 offset:51200
	ds_read_b128 v[212:215], v176 offset:51200
	s_mov_b32 m0, s77
	ds_read_b128 v[216:219], v178 offset:32768
	ds_read_b128 v[220:223], v178 offset:34816
	ds_read_b128 v[224:227], v179 offset:32768
	ds_read_b128 v[228:231], v179 offset:34816
	ds_read_b128 v[232:235], v178 offset:36864
	ds_read_b128 v[236:239], v178 offset:38912
	ds_read_b128 v[240:243], v179 offset:36864
	ds_read_b128 v[244:247], v179 offset:38912
	global_load_lds_dwordx4 v166, s[70:71]
	s_mov_b32 m0, s78
	s_nop 0
	global_load_lds_dwordx4 v164, s[70:71]
	s_mov_b32 m0, s79
	s_nop 0
	global_load_lds_dwordx4 v162, s[70:71]
	s_mov_b32 m0, s80
	s_nop 0
	global_load_lds_dwordx4 v160, s[70:71]
	s_waitcnt vmcnt(8)
	s_waitcnt lgkmcnt(0)
	s_barrier
	s_setprio 1
	s_waitcnt lgkmcnt(0)
	v_mfma_f32_16x16x32_bf16 v[126:129], v[184:187], v[216:219], v[126:129]
	v_mfma_f32_16x16x32_bf16 v[122:125], v[192:195], v[216:219], v[122:125]
	v_mfma_f32_16x16x32_bf16 v[118:121], v[184:187], v[220:223], v[118:121]
	v_mfma_f32_16x16x32_bf16 v[114:117], v[192:195], v[220:223], v[114:117]
	v_mfma_f32_16x16x32_bf16 v[110:113], v[184:187], v[232:235], v[110:113]
	v_mfma_f32_16x16x32_bf16 v[106:109], v[192:195], v[232:235], v[106:109]
	v_mfma_f32_16x16x32_bf16 v[102:105], v[184:187], v[236:239], v[102:105]
	v_mfma_f32_16x16x32_bf16 v[98:101], v[192:195], v[236:239], v[98:101]
	v_mfma_f32_16x16x32_bf16 v[126:129], v[188:191], v[224:227], v[126:129]
	v_mfma_f32_16x16x32_bf16 v[122:125], v[196:199], v[224:227], v[122:125]
	v_mfma_f32_16x16x32_bf16 v[118:121], v[188:191], v[228:231], v[118:121]
	v_mfma_f32_16x16x32_bf16 v[114:117], v[196:199], v[228:231], v[114:117]
	v_mfma_f32_16x16x32_bf16 v[110:113], v[188:191], v[240:243], v[110:113]
	v_mfma_f32_16x16x32_bf16 v[106:109], v[196:199], v[240:243], v[106:109]
	v_mfma_f32_16x16x32_bf16 v[102:105], v[188:191], v[244:247], v[102:105]
	v_mfma_f32_16x16x32_bf16 v[98:101], v[196:199], v[244:247], v[98:101]
	s_setprio 0
	s_setprio 1
	v_mfma_f32_16x16x32_bf16 v[62:65], v[200:203], v[216:219], v[62:65]
	v_mfma_f32_16x16x32_bf16 v[58:61], v[208:211], v[216:219], v[58:61]
	v_mfma_f32_16x16x32_bf16 v[54:57], v[200:203], v[220:223], v[54:57]
	v_mfma_f32_16x16x32_bf16 v[50:53], v[208:211], v[220:223], v[50:53]
	v_mfma_f32_16x16x32_bf16 v[46:49], v[200:203], v[232:235], v[46:49]
	v_mfma_f32_16x16x32_bf16 v[42:45], v[208:211], v[232:235], v[42:45]
	v_mfma_f32_16x16x32_bf16 v[38:41], v[200:203], v[236:239], v[38:41]
	v_mfma_f32_16x16x32_bf16 v[34:37], v[208:211], v[236:239], v[34:37]
	v_mfma_f32_16x16x32_bf16 v[62:65], v[204:207], v[224:227], v[62:65]
	v_mfma_f32_16x16x32_bf16 v[58:61], v[212:215], v[224:227], v[58:61]
	v_mfma_f32_16x16x32_bf16 v[54:57], v[204:207], v[228:231], v[54:57]
	v_mfma_f32_16x16x32_bf16 v[50:53], v[212:215], v[228:231], v[50:53]
	v_mfma_f32_16x16x32_bf16 v[46:49], v[204:207], v[240:243], v[46:49]
	v_mfma_f32_16x16x32_bf16 v[42:45], v[212:215], v[240:243], v[42:45]
	v_mfma_f32_16x16x32_bf16 v[38:41], v[204:207], v[244:247], v[38:41]
	v_mfma_f32_16x16x32_bf16 v[34:37], v[212:215], v[244:247], v[34:37]
	s_setprio 0
	s_barrier
	s_add_i32 s70, s92, s76
	v_lshl_add_u64 v[240:241], v[248:249], 0, s[8:9]
	s_mov_b32 m0, s70
	ds_read_b128 v[160:163], v178 offset:49152
	ds_read_b128 v[164:167], v178 offset:51200
	ds_read_b128 v[216:219], v179 offset:49152
	ds_read_b128 v[220:223], v179 offset:51200
	ds_read_b128 v[224:227], v178 offset:53248
	ds_read_b128 v[228:231], v178 offset:55296
	ds_read_b128 v[232:235], v179 offset:53248
	ds_read_b128 v[236:239], v179 offset:55296
	global_load_lds_dwordx4 v[240:241], off
	s_add_i32 m0, s70, 0x2000
	s_add_u32 s68, s68, 0x80080
	v_lshl_add_u64 v[240:241], v[250:251], 0, s[8:9]
	s_addc_u32 s69, s69, 0
	s_add_i32 s70, s94, s76
	global_load_lds_dwordx4 v[240:241], off
	s_mov_b32 m0, s70
	s_nop 0
	global_load_lds_dwordx4 v142, s[68:69]
	s_add_i32 m0, s70, 0x2000
	s_nop 0
	global_load_lds_dwordx4 v144, s[68:69]
	s_waitcnt vmcnt(6)
	s_waitcnt lgkmcnt(0)
	s_barrier
	s_setprio 1
	s_waitcnt lgkmcnt(0)
	v_mfma_f32_16x16x32_bf16 v[94:97], v[184:187], v[160:163], v[94:97]
	v_mfma_f32_16x16x32_bf16 v[90:93], v[192:195], v[160:163], v[90:93]
	v_mfma_f32_16x16x32_bf16 v[86:89], v[184:187], v[164:167], v[86:89]
	v_mfma_f32_16x16x32_bf16 v[82:85], v[192:195], v[164:167], v[82:85]
	v_mfma_f32_16x16x32_bf16 v[78:81], v[184:187], v[224:227], v[78:81]
	v_mfma_f32_16x16x32_bf16 v[74:77], v[192:195], v[224:227], v[74:77]
	v_mfma_f32_16x16x32_bf16 v[70:73], v[184:187], v[228:231], v[70:73]
	v_mfma_f32_16x16x32_bf16 v[66:69], v[192:195], v[228:231], v[66:69]
	v_mfma_f32_16x16x32_bf16 v[94:97], v[188:191], v[216:219], v[94:97]
	v_mfma_f32_16x16x32_bf16 v[90:93], v[196:199], v[216:219], v[90:93]
	v_mfma_f32_16x16x32_bf16 v[86:89], v[188:191], v[220:223], v[86:89]
	v_mfma_f32_16x16x32_bf16 v[82:85], v[196:199], v[220:223], v[82:85]
	v_mfma_f32_16x16x32_bf16 v[78:81], v[188:191], v[232:235], v[78:81]
	v_mfma_f32_16x16x32_bf16 v[74:77], v[196:199], v[232:235], v[74:77]
	v_mfma_f32_16x16x32_bf16 v[70:73], v[188:191], v[236:239], v[70:73]
	v_mfma_f32_16x16x32_bf16 v[66:69], v[196:199], v[236:239], v[66:69]
	s_setprio 0
	s_setprio 1
	v_mfma_f32_16x16x32_bf16 v[30:33], v[200:203], v[160:163], v[30:33]
	v_mfma_f32_16x16x32_bf16 v[26:29], v[208:211], v[160:163], v[26:29]
	v_mfma_f32_16x16x32_bf16 v[22:25], v[200:203], v[164:167], v[22:25]
	v_mfma_f32_16x16x32_bf16 v[18:21], v[208:211], v[164:167], v[18:21]
	v_mfma_f32_16x16x32_bf16 v[14:17], v[200:203], v[224:227], v[14:17]
	v_mfma_f32_16x16x32_bf16 v[10:13], v[208:211], v[224:227], v[10:13]
	v_mfma_f32_16x16x32_bf16 v[6:9], v[200:203], v[228:231], v[6:9]
	v_mfma_f32_16x16x32_bf16 v[2:5], v[208:211], v[228:231], v[2:5]
	v_mfma_f32_16x16x32_bf16 v[30:33], v[204:207], v[216:219], v[30:33]
	v_mfma_f32_16x16x32_bf16 v[26:29], v[212:215], v[216:219], v[26:29]
	v_mfma_f32_16x16x32_bf16 v[22:25], v[204:207], v[220:223], v[22:25]
	v_mfma_f32_16x16x32_bf16 v[18:21], v[212:215], v[220:223], v[18:21]
	v_mfma_f32_16x16x32_bf16 v[14:17], v[204:207], v[232:235], v[14:17]
	v_mfma_f32_16x16x32_bf16 v[10:13], v[212:215], v[232:235], v[10:13]
	v_mfma_f32_16x16x32_bf16 v[6:9], v[204:207], v[236:239], v[6:9]
	v_mfma_f32_16x16x32_bf16 v[2:5], v[212:215], v[236:239], v[2:5]
	s_setprio 0
	s_barrier
	s_add_i32 s72, s72, 2
	s_add_u32 s66, s66, 0x100
	s_addc_u32 s67, s67, 0
	s_cmp_gt_u32 s72, 29
	s_cbranch_scc1 .LBB0_105

.Lp3_blk3:
	ds_read_b128 v[184:187], v174 offset:32768
	ds_read_b128 v[188:191], v175 offset:32768
	ds_read_b128 v[192:195], v174 offset:34816
	ds_read_b128 v[196:199], v175 offset:34816
	ds_read_b128 v[200:203], v174 offset:49152
	ds_read_b128 v[204:207], v175 offset:49152
	ds_read_b128 v[208:211], v174 offset:51200
	ds_read_b128 v[212:215], v175 offset:51200
	s_mov_b32 m0, s39
	ds_read_b128 v[216:219], v177 offset:32768
	ds_read_b128 v[220:223], v177 offset:34816
	ds_read_b128 v[224:227], v178 offset:32768
	ds_read_b128 v[228:231], v178 offset:34816
	ds_read_b128 v[232:235], v177 offset:36864
	ds_read_b128 v[236:239], v177 offset:38912
	ds_read_b128 v[240:243], v178 offset:36864
	ds_read_b128 v[244:247], v178 offset:38912
	global_load_lds_dwordx4 v166, s[34:35]
	s_mov_b32 m0, s40
	s_nop 0
	global_load_lds_dwordx4 v164, s[34:35]
	s_mov_b32 m0, s41
	s_nop 0
	global_load_lds_dwordx4 v162, s[34:35]
	s_mov_b32 m0, s42
	s_nop 0
	global_load_lds_dwordx4 v160, s[34:35]
	s_waitcnt vmcnt(8)
	s_waitcnt lgkmcnt(0)
	s_barrier
	s_setprio 1
	s_waitcnt lgkmcnt(0)
	v_mfma_f32_16x16x32_bf16 v[126:129], v[184:187], v[216:219], v[126:129]
	v_mfma_f32_16x16x32_bf16 v[122:125], v[192:195], v[216:219], v[122:125]
	v_mfma_f32_16x16x32_bf16 v[118:121], v[184:187], v[220:223], v[118:121]
	v_mfma_f32_16x16x32_bf16 v[114:117], v[192:195], v[220:223], v[114:117]
	v_mfma_f32_16x16x32_bf16 v[110:113], v[184:187], v[232:235], v[110:113]
	v_mfma_f32_16x16x32_bf16 v[102:105], v[192:195], v[232:235], v[102:105]
	v_mfma_f32_16x16x32_bf16 v[94:97], v[184:187], v[236:239], v[94:97]
	v_mfma_f32_16x16x32_bf16 v[86:89], v[192:195], v[236:239], v[86:89]
	v_mfma_f32_16x16x32_bf16 v[126:129], v[188:191], v[224:227], v[126:129]
	v_mfma_f32_16x16x32_bf16 v[122:125], v[196:199], v[224:227], v[122:125]
	v_mfma_f32_16x16x32_bf16 v[118:121], v[188:191], v[228:231], v[118:121]
	v_mfma_f32_16x16x32_bf16 v[114:117], v[196:199], v[228:231], v[114:117]
	v_mfma_f32_16x16x32_bf16 v[110:113], v[188:191], v[240:243], v[110:113]
	v_mfma_f32_16x16x32_bf16 v[102:105], v[196:199], v[240:243], v[102:105]
	v_mfma_f32_16x16x32_bf16 v[94:97], v[188:191], v[244:247], v[94:97]
	v_mfma_f32_16x16x32_bf16 v[86:89], v[196:199], v[244:247], v[86:89]
	s_setprio 0
	s_setprio 1
	v_mfma_f32_16x16x32_bf16 v[106:109], v[200:203], v[216:219], v[106:109]
	v_mfma_f32_16x16x32_bf16 v[98:101], v[208:211], v[216:219], v[98:101]
	v_mfma_f32_16x16x32_bf16 v[90:93], v[200:203], v[220:223], v[90:93]
	v_mfma_f32_16x16x32_bf16 v[82:85], v[208:211], v[220:223], v[82:85]
	v_mfma_f32_16x16x32_bf16 v[78:81], v[200:203], v[232:235], v[78:81]
	v_mfma_f32_16x16x32_bf16 v[74:77], v[208:211], v[232:235], v[74:77]
	v_mfma_f32_16x16x32_bf16 v[70:73], v[200:203], v[236:239], v[70:73]
	v_mfma_f32_16x16x32_bf16 v[66:69], v[208:211], v[236:239], v[66:69]
	v_mfma_f32_16x16x32_bf16 v[106:109], v[204:207], v[224:227], v[106:109]
	v_mfma_f32_16x16x32_bf16 v[98:101], v[212:215], v[224:227], v[98:101]
	v_mfma_f32_16x16x32_bf16 v[90:93], v[204:207], v[228:231], v[90:93]
	v_mfma_f32_16x16x32_bf16 v[82:85], v[212:215], v[228:231], v[82:85]
	v_mfma_f32_16x16x32_bf16 v[78:81], v[204:207], v[240:243], v[78:81]
	v_mfma_f32_16x16x32_bf16 v[74:77], v[212:215], v[240:243], v[74:77]
	v_mfma_f32_16x16x32_bf16 v[70:73], v[204:207], v[244:247], v[70:73]
	v_mfma_f32_16x16x32_bf16 v[66:69], v[212:215], v[244:247], v[66:69]
	s_setprio 0
	s_barrier
	s_add_i32 s34, s65, s33
	v_lshl_add_u64 v[240:241], v[248:249], 0, s[8:9]
	s_mov_b32 m0, s34
	ds_read_b128 v[160:163], v177 offset:49152
	ds_read_b128 v[164:167], v177 offset:51200
	ds_read_b128 v[216:219], v178 offset:49152
	ds_read_b128 v[220:223], v178 offset:51200
	ds_read_b128 v[224:227], v177 offset:53248
	ds_read_b128 v[228:231], v177 offset:55296
	ds_read_b128 v[232:235], v178 offset:53248
	ds_read_b128 v[236:239], v178 offset:55296
	global_load_lds_dwordx4 v[240:241], off
	s_add_i32 m0, s34, 0x2000
	s_add_u32 s30, s30, 0x80080
	v_lshl_add_u64 v[240:241], v[250:251], 0, s[8:9]
	s_addc_u32 s31, s31, 0
	s_add_i32 s34, s67, s33
	global_load_lds_dwordx4 v[240:241], off
	s_mov_b32 m0, s34
	s_nop 0
	global_load_lds_dwordx4 v146, s[30:31]
	s_add_i32 m0, s34, 0x2000
	s_nop 0
	global_load_lds_dwordx4 v148, s[30:31]
	s_waitcnt vmcnt(6)
	s_waitcnt lgkmcnt(0)
	s_barrier
	s_setprio 1
	s_waitcnt lgkmcnt(0)
	v_mfma_f32_16x16x32_bf16 v[62:65], v[184:187], v[160:163], v[62:65]
	v_mfma_f32_16x16x32_bf16 v[58:61], v[192:195], v[160:163], v[58:61]
	v_mfma_f32_16x16x32_bf16 v[50:53], v[184:187], v[164:167], v[50:53]
	v_mfma_f32_16x16x32_bf16 v[42:45], v[192:195], v[164:167], v[42:45]
	v_mfma_f32_16x16x32_bf16 v[34:37], v[184:187], v[224:227], v[34:37]
	v_mfma_f32_16x16x32_bf16 v[26:29], v[192:195], v[224:227], v[26:29]
	v_mfma_f32_16x16x32_bf16 v[18:21], v[184:187], v[228:231], v[18:21]
	v_mfma_f32_16x16x32_bf16 v[10:13], v[192:195], v[228:231], v[10:13]
	v_mfma_f32_16x16x32_bf16 v[62:65], v[188:191], v[216:219], v[62:65]
	v_mfma_f32_16x16x32_bf16 v[58:61], v[196:199], v[216:219], v[58:61]
	v_mfma_f32_16x16x32_bf16 v[50:53], v[188:191], v[220:223], v[50:53]
	v_mfma_f32_16x16x32_bf16 v[42:45], v[196:199], v[220:223], v[42:45]
	v_mfma_f32_16x16x32_bf16 v[34:37], v[188:191], v[232:235], v[34:37]
	v_mfma_f32_16x16x32_bf16 v[26:29], v[196:199], v[232:235], v[26:29]
	v_mfma_f32_16x16x32_bf16 v[18:21], v[188:191], v[236:239], v[18:21]
	v_mfma_f32_16x16x32_bf16 v[10:13], v[196:199], v[236:239], v[10:13]
	s_setprio 0
	s_setprio 1
	v_mfma_f32_16x16x32_bf16 v[54:57], v[200:203], v[160:163], v[54:57]
	v_mfma_f32_16x16x32_bf16 v[46:49], v[208:211], v[160:163], v[46:49]
	v_mfma_f32_16x16x32_bf16 v[38:41], v[200:203], v[164:167], v[38:41]
	v_mfma_f32_16x16x32_bf16 v[30:33], v[208:211], v[164:167], v[30:33]
	v_mfma_f32_16x16x32_bf16 v[22:25], v[200:203], v[224:227], v[22:25]
	v_mfma_f32_16x16x32_bf16 v[14:17], v[208:211], v[224:227], v[14:17]
	v_mfma_f32_16x16x32_bf16 v[6:9], v[200:203], v[228:231], v[6:9]
	v_mfma_f32_16x16x32_bf16 v[2:5], v[208:211], v[228:231], v[2:5]
	v_mfma_f32_16x16x32_bf16 v[54:57], v[204:207], v[216:219], v[54:57]
	v_mfma_f32_16x16x32_bf16 v[46:49], v[212:215], v[216:219], v[46:49]
	v_mfma_f32_16x16x32_bf16 v[38:41], v[204:207], v[220:223], v[38:41]
	v_mfma_f32_16x16x32_bf16 v[30:33], v[212:215], v[220:223], v[30:33]
	v_mfma_f32_16x16x32_bf16 v[22:25], v[204:207], v[232:235], v[22:25]
	v_mfma_f32_16x16x32_bf16 v[14:17], v[212:215], v[232:235], v[14:17]
	v_mfma_f32_16x16x32_bf16 v[6:9], v[204:207], v[236:239], v[6:9]
	v_mfma_f32_16x16x32_bf16 v[2:5], v[212:215], v[236:239], v[2:5]
	s_setprio 0
	s_barrier
	s_add_i32 s76, s76, 2
	s_add_u32 s28, s28, 0x100
	s_addc_u32 s29, s29, 0
	s_cmp_gt_u32 s76, 29
	s_cbranch_scc1 .LBB0_389

.Lp6_blk3:
	ds_read_b128 v[2:5], v208 offset:32768
	ds_read_b128 v[6:9], v209 offset:32768
	ds_read_b128 v[10:13], v208 offset:34816
	ds_read_b128 v[14:17], v209 offset:34816
	ds_read_b128 v[18:21], v208 offset:49152
	ds_read_b128 v[22:25], v209 offset:49152
	ds_read_b128 v[26:29], v208 offset:51200
	ds_read_b128 v[30:33], v209 offset:51200
	s_mov_b32 m0, s35
	ds_read_b128 v[218:221], v211 offset:32768
	ds_read_b128 v[226:229], v211 offset:34816
	ds_read_b128 v[222:225], v212 offset:32768
	ds_read_b128 v[230:233], v212 offset:34816
	ds_read_b128 v[234:237], v211 offset:36864
	ds_read_b128 v[242:245], v211 offset:38912
	ds_read_b128 v[238:241], v212 offset:36864
	ds_read_b128 v[246:249], v212 offset:38912
	global_load_lds_dwordx4 v198, s[44:45]
	s_mov_b32 m0, s55
	s_nop 0
	global_load_lds_dwordx4 v196, s[44:45]
	s_mov_b32 m0, s64
	s_nop 0
	global_load_lds_dwordx4 v194, s[44:45]
	s_mov_b32 m0, s65
	s_nop 0
	global_load_lds_dwordx4 v192, s[44:45]
	s_waitcnt vmcnt(8)
	s_waitcnt lgkmcnt(0)
	s_barrier
	s_setprio 1
	s_waitcnt lgkmcnt(0)
	v_mfma_f32_16x16x128_f8f6f4 v[158:161], v[2:9], v[218:225], v[158:161]
	v_mfma_f32_16x16x128_f8f6f4 v[154:157], v[10:17], v[218:225], v[154:157]
	v_mfma_f32_16x16x128_f8f6f4 v[150:153], v[2:9], v[226:233], v[150:153]
	v_mfma_f32_16x16x128_f8f6f4 v[146:149], v[10:17], v[226:233], v[146:149]
	v_mfma_f32_16x16x128_f8f6f4 v[126:129], v[2:9], v[234:241], v[126:129]
	v_mfma_f32_16x16x128_f8f6f4 v[122:125], v[10:17], v[234:241], v[122:125]
	v_mfma_f32_16x16x128_f8f6f4 v[110:113], v[2:9], v[242:249], v[110:113]
	v_mfma_f32_16x16x128_f8f6f4 v[106:109], v[10:17], v[242:249], v[106:109]
	s_setprio 0
	s_setprio 1
	v_mfma_f32_16x16x128_f8f6f4 v[142:145], v[18:25], v[218:225], v[142:145]
	v_mfma_f32_16x16x128_f8f6f4 v[138:141], v[26:33], v[218:225], v[138:141]
	v_mfma_f32_16x16x128_f8f6f4 v[134:137], v[18:25], v[226:233], v[134:137]
	v_mfma_f32_16x16x128_f8f6f4 v[130:133], v[26:33], v[226:233], v[130:133]
	v_mfma_f32_16x16x128_f8f6f4 v[118:121], v[18:25], v[234:241], v[118:121]
	v_mfma_f32_16x16x128_f8f6f4 v[114:117], v[26:33], v[234:241], v[114:117]
	v_mfma_f32_16x16x128_f8f6f4 v[102:105], v[18:25], v[242:249], v[102:105]
	v_mfma_f32_16x16x128_f8f6f4 v[98:101], v[26:33], v[242:249], v[98:101]
	s_setprio 0
	s_barrier
	s_add_i32 s44, s72, s33
	v_lshl_add_u64 v[200:201], v[200:201], 0, s[10:11]
	s_mov_b32 m0, s44
	ds_read_b128 v[192:195], v211 offset:49152
	ds_read_b128 v[218:221], v211 offset:51200
	ds_read_b128 v[196:199], v212 offset:49152
	ds_read_b128 v[222:225], v212 offset:51200
	ds_read_b128 v[226:229], v211 offset:53248
	ds_read_b128 v[234:237], v211 offset:55296
	ds_read_b128 v[230:233], v212 offset:53248
	ds_read_b128 v[238:241], v212 offset:55296
	global_load_lds_dwordx4 v[200:201], off
	s_add_i32 m0, s44, 0x2000
	s_add_u32 s42, s42, 0x40080
	v_lshl_add_u64 v[200:201], v[202:203], 0, s[10:11]
	s_addc_u32 s43, s43, 0
	s_add_i32 s44, s74, s33
	global_load_lds_dwordx4 v[200:201], off
	s_mov_b32 m0, s44
	s_nop 0
	global_load_lds_dwordx4 v164, s[42:43]
	s_add_i32 m0, s44, 0x2000
	s_nop 0
	global_load_lds_dwordx4 v166, s[42:43]
	s_waitcnt vmcnt(6)
	s_waitcnt lgkmcnt(0)
	s_barrier
	s_setprio 1
	s_waitcnt lgkmcnt(0)
	v_mfma_f32_16x16x128_f8f6f4 v[94:97], v[2:9], v[192:199], v[94:97]
	v_mfma_f32_16x16x128_f8f6f4 v[90:93], v[10:17], v[192:199], v[90:93]
	v_mfma_f32_16x16x128_f8f6f4 v[78:81], v[2:9], v[218:225], v[78:81]
	v_mfma_f32_16x16x128_f8f6f4 v[74:77], v[10:17], v[218:225], v[74:77]
	v_mfma_f32_16x16x128_f8f6f4 v[62:65], v[2:9], v[226:233], v[62:65]
	v_mfma_f32_16x16x128_f8f6f4 v[58:61], v[10:17], v[226:233], v[58:61]
	v_mfma_f32_16x16x128_f8f6f4 v[46:49], v[2:9], v[234:241], v[46:49]
	v_mfma_f32_16x16x128_f8f6f4 v[42:45], v[10:17], v[234:241], v[42:45]
	s_setprio 0
	s_setprio 1
	v_mfma_f32_16x16x128_f8f6f4 v[86:89], v[18:25], v[192:199], v[86:89]
	v_mfma_f32_16x16x128_f8f6f4 v[82:85], v[26:33], v[192:199], v[82:85]
	v_mfma_f32_16x16x128_f8f6f4 v[70:73], v[18:25], v[218:225], v[70:73]
	v_mfma_f32_16x16x128_f8f6f4 v[66:69], v[26:33], v[218:225], v[66:69]
	v_mfma_f32_16x16x128_f8f6f4 v[54:57], v[18:25], v[226:233], v[54:57]
	v_mfma_f32_16x16x128_f8f6f4 v[50:53], v[26:33], v[226:233], v[50:53]
	v_mfma_f32_16x16x128_f8f6f4 v[38:41], v[18:25], v[234:241], v[38:41]
	v_mfma_f32_16x16x128_f8f6f4 v[34:37], v[26:33], v[234:241], v[34:37]
	s_setprio 0
	s_barrier
	s_add_i32 s83, s83, 2
	s_add_u32 s40, s40, 0x100
	s_addc_u32 s41, s41, 0
	s_cmp_gt_u32 s83, 13
	s_cbranch_scc1 .LBB0_781

.Lp7_blk3:
	ds_read_b128 v[2:5], v210 offset:32768
	ds_read_b128 v[6:9], v211 offset:32768
	ds_read_b128 v[10:13], v210 offset:34816
	ds_read_b128 v[14:17], v211 offset:34816
	ds_read_b128 v[18:21], v210 offset:49152
	ds_read_b128 v[22:25], v211 offset:49152
	ds_read_b128 v[26:29], v210 offset:51200
	ds_read_b128 v[30:33], v211 offset:51200
	s_mov_b32 m0, s41
	ds_read_b128 v[220:223], v213 offset:32768
	ds_read_b128 v[228:231], v213 offset:34816
	ds_read_b128 v[224:227], v214 offset:32768
	ds_read_b128 v[232:235], v214 offset:34816
	ds_read_b128 v[236:239], v213 offset:36864
	ds_read_b128 v[244:247], v213 offset:38912
	ds_read_b128 v[240:243], v214 offset:36864
	ds_read_b128 v[248:251], v214 offset:38912
	global_load_lds_dwordx4 v198, s[48:49]
	s_mov_b32 m0, s53
	s_nop 0
	global_load_lds_dwordx4 v196, s[48:49]
	s_mov_b32 m0, s54
	s_nop 0
	global_load_lds_dwordx4 v194, s[48:49]
	s_mov_b32 m0, s55
	s_nop 0
	global_load_lds_dwordx4 v192, s[48:49]
	s_waitcnt vmcnt(8)
	s_waitcnt lgkmcnt(0)
	s_barrier
	s_setprio 1
	s_waitcnt lgkmcnt(0)
	v_mfma_f32_16x16x128_f8f6f4 v[158:161], v[2:9], v[220:227], v[158:161]
	v_mfma_f32_16x16x128_f8f6f4 v[154:157], v[10:17], v[220:227], v[154:157]
	v_mfma_f32_16x16x128_f8f6f4 v[150:153], v[2:9], v[228:235], v[150:153]
	v_mfma_f32_16x16x128_f8f6f4 v[146:149], v[10:17], v[228:235], v[146:149]
	v_mfma_f32_16x16x128_f8f6f4 v[142:145], v[2:9], v[236:243], v[142:145]
	v_mfma_f32_16x16x128_f8f6f4 v[138:141], v[10:17], v[236:243], v[138:141]
	v_mfma_f32_16x16x128_f8f6f4 v[134:137], v[2:9], v[244:251], v[134:137]
	v_mfma_f32_16x16x128_f8f6f4 v[130:133], v[10:17], v[244:251], v[130:133]
	s_setprio 0
	s_setprio 1
	v_mfma_f32_16x16x128_f8f6f4 v[102:105], v[18:25], v[220:227], v[102:105]
	v_mfma_f32_16x16x128_f8f6f4 v[94:97], v[26:33], v[220:227], v[94:97]
	v_mfma_f32_16x16x128_f8f6f4 v[86:89], v[18:25], v[228:235], v[86:89]
	v_mfma_f32_16x16x128_f8f6f4 v[82:85], v[26:33], v[228:235], v[82:85]
	v_mfma_f32_16x16x128_f8f6f4 v[78:81], v[18:25], v[236:243], v[78:81]
	v_mfma_f32_16x16x128_f8f6f4 v[74:77], v[26:33], v[236:243], v[74:77]
	v_mfma_f32_16x16x128_f8f6f4 v[70:73], v[18:25], v[244:251], v[70:73]
	v_mfma_f32_16x16x128_f8f6f4 v[66:69], v[26:33], v[244:251], v[66:69]
	s_setprio 0
	s_barrier
	s_add_i32 s48, s70, s51
	v_lshl_add_u64 v[200:201], v[200:201], 0, s[10:11]
	s_mov_b32 m0, s48
	ds_read_b128 v[192:195], v213 offset:49152
	ds_read_b128 v[220:223], v213 offset:51200
	ds_read_b128 v[196:199], v214 offset:49152
	ds_read_b128 v[224:227], v214 offset:51200
	ds_read_b128 v[228:231], v213 offset:53248
	ds_read_b128 v[236:239], v213 offset:55296
	ds_read_b128 v[232:235], v214 offset:53248
	ds_read_b128 v[240:243], v214 offset:55296
	global_load_lds_dwordx4 v[200:201], off
	s_add_i32 m0, s48, 0x2000
	s_add_u32 s46, s46, 0x40080
	v_lshl_add_u64 v[200:201], v[202:203], 0, s[10:11]
	s_addc_u32 s47, s47, 0
	s_add_i32 s48, s72, s51
	global_load_lds_dwordx4 v[200:201], off
	s_mov_b32 m0, s48
	s_nop 0
	global_load_lds_dwordx4 v162, s[46:47]
	s_add_i32 m0, s48, 0x2000
	s_nop 0
	global_load_lds_dwordx4 v164, s[46:47]
	s_waitcnt vmcnt(6)
	s_waitcnt lgkmcnt(0)
	s_barrier
	s_setprio 1
	s_waitcnt lgkmcnt(0)
	v_mfma_f32_16x16x128_f8f6f4 v[126:129], v[2:9], v[192:199], v[126:129]
	v_mfma_f32_16x16x128_f8f6f4 v[122:125], v[10:17], v[192:199], v[122:125]
	v_mfma_f32_16x16x128_f8f6f4 v[118:121], v[2:9], v[220:227], v[118:121]
	v_mfma_f32_16x16x128_f8f6f4 v[114:117], v[10:17], v[220:227], v[114:117]
	v_mfma_f32_16x16x128_f8f6f4 v[110:113], v[2:9], v[228:235], v[110:113]
	v_mfma_f32_16x16x128_f8f6f4 v[106:109], v[10:17], v[228:235], v[106:109]
	v_mfma_f32_16x16x128_f8f6f4 v[98:101], v[2:9], v[236:243], v[98:101]
	v_mfma_f32_16x16x128_f8f6f4 v[90:93], v[10:17], v[236:243], v[90:93]
	s_setprio 0
	s_setprio 1
	v_mfma_f32_16x16x128_f8f6f4 v[62:65], v[18:25], v[192:199], v[62:65]
	v_mfma_f32_16x16x128_f8f6f4 v[58:61], v[26:33], v[192:199], v[58:61]
	v_mfma_f32_16x16x128_f8f6f4 v[54:57], v[18:25], v[220:227], v[54:57]
	v_mfma_f32_16x16x128_f8f6f4 v[50:53], v[26:33], v[220:227], v[50:53]
	v_mfma_f32_16x16x128_f8f6f4 v[46:49], v[18:25], v[228:235], v[46:49]
	v_mfma_f32_16x16x128_f8f6f4 v[42:45], v[26:33], v[228:235], v[42:45]
	v_mfma_f32_16x16x128_f8f6f4 v[38:41], v[18:25], v[236:243], v[38:41]
	v_mfma_f32_16x16x128_f8f6f4 v[34:37], v[26:33], v[236:243], v[34:37]
	s_setprio 0
	s_barrier
	s_add_i32 s43, s43, 2
	s_add_u32 s44, s44, 0x100
	s_addc_u32 s45, s45, 0
	s_cmp_gt_u32 s43, 13
	s_cbranch_scc1 .LBB0_866
